# v79 + grid barrier: each workgroup's agent-scope L1 invalidate issued right after its arrival atomic (overlaps the wait for the release / the leader's L2 write-back) instead of after the release
# speedup vs baseline: 1.0249x; 1.0104x over previous
.LBB0_97:
	s_or_b64 exec, exec, s[8:9]
	v_cvt_f32_u32_e32 v5, v3
	buffer_inv sc1
	s_waitcnt vmcnt(1)
	v_readfirstlane_b32 s2, v4
	v_sub_u32_e32 v4, 0, v3
	v_rcp_iflag_f32_e32 v5, v5
	v_add_u32_e32 v6, s2, v2
	v_mul_f32_e32 v5, 0x4f7ffffe, v5
	v_cvt_u32_f32_e32 v5, v5
	v_mul_lo_u32 v2, v4, v5
	v_mul_hi_u32 v2, v5, v2
	v_add_u32_e32 v2, v5, v2
	v_mul_hi_u32 v2, v6, v2
	v_mul_lo_u32 v4, v2, v3
	v_sub_u32_e32 v4, v6, v4
	v_add_u32_e32 v5, 1, v2
	v_cmp_ge_u32_e32 vcc, v4, v3
	s_nop 1
	v_cndmask_b32_e32 v2, v2, v5, vcc
	v_sub_u32_e32 v5, v4, v3
	v_cndmask_b32_e32 v4, v4, v5, vcc
	v_add_u32_e32 v5, 1, v2
	v_cmp_ge_u32_e32 vcc, v4, v3
	v_add_u32_e32 v4, 1, v6
	s_nop 0
	v_cndmask_b32_e32 v2, v2, v5, vcc
	v_mul_lo_u32 v5, v3, v2
	v_add_u32_e32 v3, v5, v3
	v_cmp_ne_u32_e32 vcc, v4, v3
	s_and_saveexec_b64 s[2:3], vcc
	s_xor_b64 s[8:9], exec, s[2:3]
	s_cbranch_execz .LBB0_111
	s_waitcnt lgkmcnt(0)
	v_mov_b32_e32 v1, 0x2000
	global_load_dword v1, v1, s[6:7] offset:1024 sc1
	s_add_u32 s14, s6, 0x2400
	s_addc_u32 s15, s7, 0
	s_waitcnt vmcnt(0)
	v_cmp_eq_u32_e32 vcc, v1, v2
	s_and_saveexec_b64 s[10:11], vcc
	s_cbranch_execz .LBB0_110
	s_add_u32 s12, s0, 0x4200
	s_addc_u32 s13, s1, 0
	s_mov_b32 s24, 1
	s_mov_b64 s[16:17], 0
	v_mov_b32_e32 v1, 0
	s_branch .LBB0_101

.LBB0_110:
	s_or_b64 exec, exec, s[10:11]
	s_waitcnt vmcnt(0)
	s_waitcnt vmcnt(0)

.LBB0_128:
	s_or_b64 exec, exec, s[8:9]
	s_mov_b64 s[2:3], exec
	v_mbcnt_lo_u32_b32 v1, s2, 0
	v_mbcnt_hi_u32_b32 v1, s3, v1
	v_cmp_eq_u32_e32 vcc, 0, v1
	s_waitcnt vmcnt(0)
	s_and_saveexec_b64 s[8:9], vcc
	s_cbranch_execz .LBB0_130
	s_bcnt1_i32_b64 s2, s[2:3]
	v_mov_b32_e32 v1, 0x2000
	v_mov_b32_e32 v2, s2
	global_atomic_add v1, v2, s[6:7] offset:1024

.LBB0_375:
	s_or_b64 exec, exec, s[26:27]
	v_cvt_f32_u32_e32 v6, v4
	buffer_inv sc1
	s_waitcnt vmcnt(1)
	v_readfirstlane_b32 s3, v5
	v_sub_u32_e32 v5, 0, v4
	v_rcp_iflag_f32_e32 v6, v6
	v_add_u32_e32 v7, s3, v3
	v_mul_f32_e32 v6, 0x4f7ffffe, v6
	v_cvt_u32_f32_e32 v6, v6
	v_mul_lo_u32 v3, v5, v6
	v_mul_hi_u32 v3, v6, v3
	v_add_u32_e32 v3, v6, v3
	v_mul_hi_u32 v3, v7, v3
	v_mul_lo_u32 v5, v3, v4
	v_sub_u32_e32 v5, v7, v5
	v_add_u32_e32 v6, 1, v3
	v_cmp_ge_u32_e32 vcc, v5, v4
	s_nop 1
	v_cndmask_b32_e32 v3, v3, v6, vcc
	v_sub_u32_e32 v6, v5, v4
	v_cndmask_b32_e32 v5, v5, v6, vcc
	v_add_u32_e32 v6, 1, v3
	v_cmp_ge_u32_e32 vcc, v5, v4
	v_add_u32_e32 v5, 1, v7
	s_nop 0
	v_cndmask_b32_e32 v3, v3, v6, vcc
	v_mul_lo_u32 v6, v4, v3
	v_add_u32_e32 v4, v6, v4
	v_cmp_ne_u32_e32 vcc, v5, v4
	s_and_saveexec_b64 s[4:5], vcc
	s_xor_b64 s[36:37], exec, s[4:5]
	s_cbranch_execz .LBB0_389
	v_readlane_b32 s4, v254, 7
	v_readlane_b32 s5, v254, 8
	s_waitcnt lgkmcnt(0)
	s_nop 3
	global_load_dword v2, v67, s[4:5] sc1
	s_waitcnt vmcnt(0)
	v_cmp_eq_u32_e32 vcc, v2, v3
	s_and_saveexec_b64 s[38:39], vcc
	s_cbranch_execz .LBB0_388
	s_mov_b32 s3, 1
	s_mov_b64 s[40:41], 0
	s_branch .LBB0_379

.LBB0_388:
	s_or_b64 exec, exec, s[38:39]
	s_waitcnt vmcnt(0)
	s_waitcnt vmcnt(0)

.LBB0_406:
	s_or_b64 exec, exec, s[36:37]
	s_mov_b64 s[26:27], exec
	v_mbcnt_lo_u32_b32 v2, s26, 0
	v_mbcnt_hi_u32_b32 v2, s27, v2
	v_cmp_eq_u32_e32 vcc, 0, v2
	s_waitcnt vmcnt(0)
	s_and_saveexec_b64 s[36:37], vcc
	s_cbranch_execz .LBB0_408
	s_bcnt1_i32_b64 s3, s[26:27]
	v_readlane_b32 s4, v254, 7
	v_mov_b32_e32 v2, s3
	v_readlane_b32 s5, v254, 8
	s_nop 4
	global_atomic_add v67, v2, s[4:5]

.LBB0_754:
	s_or_b64 exec, exec, s[26:27]
	v_cvt_f32_u32_e32 v6, v4
	buffer_inv sc1
	s_waitcnt vmcnt(1)
	v_readfirstlane_b32 s2, v5
	v_sub_u32_e32 v5, 0, v4
	v_rcp_iflag_f32_e32 v6, v6
	v_add_u32_e32 v7, s2, v3
	v_mul_f32_e32 v6, 0x4f7ffffe, v6
	v_cvt_u32_f32_e32 v6, v6
	v_mul_lo_u32 v3, v5, v6
	v_mul_hi_u32 v3, v6, v3
	v_add_u32_e32 v3, v6, v3
	v_mul_hi_u32 v3, v7, v3
	v_mul_lo_u32 v5, v3, v4
	v_sub_u32_e32 v5, v7, v5
	v_add_u32_e32 v6, 1, v3
	v_cmp_ge_u32_e32 vcc, v5, v4
	s_nop 1
	v_cndmask_b32_e32 v3, v3, v6, vcc
	v_sub_u32_e32 v6, v5, v4
	v_cndmask_b32_e32 v5, v5, v6, vcc
	v_add_u32_e32 v6, 1, v3
	v_cmp_ge_u32_e32 vcc, v5, v4
	v_add_u32_e32 v5, 1, v7
	s_nop 0
	v_cndmask_b32_e32 v3, v3, v6, vcc
	v_mul_lo_u32 v6, v4, v3
	v_add_u32_e32 v4, v6, v4
	v_cmp_ne_u32_e32 vcc, v5, v4
	s_and_saveexec_b64 s[2:3], vcc
	s_xor_b64 s[36:37], exec, s[2:3]
	s_cbranch_execz .LBB0_768
	v_readlane_b32 s2, v254, 7
	v_readlane_b32 s3, v254, 8
	s_waitcnt lgkmcnt(0)
	s_nop 3
	global_load_dword v2, v67, s[2:3] sc1
	s_waitcnt vmcnt(0)
	v_cmp_eq_u32_e32 vcc, v2, v3
	s_and_saveexec_b64 s[38:39], vcc
	s_cbranch_execz .LBB0_767
	s_mov_b32 s2, 1
	s_mov_b64 s[40:41], 0
	s_branch .LBB0_758

.LBB0_785:
	s_or_b64 exec, exec, s[36:37]
	s_mov_b64 s[26:27], exec
	v_mbcnt_lo_u32_b32 v2, s26, 0
	v_mbcnt_hi_u32_b32 v2, s27, v2
	v_cmp_eq_u32_e32 vcc, 0, v2
	s_waitcnt vmcnt(0)
	s_and_saveexec_b64 s[36:37], vcc
	s_cbranch_execz .LBB0_787
	s_bcnt1_i32_b64 s2, s[26:27]
	v_mov_b32_e32 v2, s2
	v_readlane_b32 s2, v254, 7
	v_readlane_b32 s3, v254, 8
	s_nop 4
	global_atomic_add v67, v2, s[2:3]

.LBB0_1159:
	s_or_b64 exec, exec, s[26:27]
	v_cvt_f32_u32_e32 v6, v4
	buffer_inv sc1
	s_waitcnt vmcnt(1)
	v_readfirstlane_b32 s3, v5
	v_sub_u32_e32 v5, 0, v4
	v_rcp_iflag_f32_e32 v6, v6
	v_add_u32_e32 v7, s3, v3
	v_mul_f32_e32 v6, 0x4f7ffffe, v6
	v_cvt_u32_f32_e32 v6, v6
	v_mul_lo_u32 v3, v5, v6
	v_mul_hi_u32 v3, v6, v3
	v_add_u32_e32 v3, v6, v3
	v_mul_hi_u32 v3, v7, v3
	v_mul_lo_u32 v5, v3, v4
	v_sub_u32_e32 v5, v7, v5
	v_add_u32_e32 v6, 1, v3
	v_cmp_ge_u32_e32 vcc, v5, v4
	s_nop 1
	v_cndmask_b32_e32 v3, v3, v6, vcc
	v_sub_u32_e32 v6, v5, v4
	v_cndmask_b32_e32 v5, v5, v6, vcc
	v_add_u32_e32 v6, 1, v3
	v_cmp_ge_u32_e32 vcc, v5, v4
	v_add_u32_e32 v5, 1, v7
	s_nop 0
	v_cndmask_b32_e32 v3, v3, v6, vcc
	v_mul_lo_u32 v6, v4, v3
	v_add_u32_e32 v4, v6, v4
	v_cmp_ne_u32_e32 vcc, v5, v4
	s_and_saveexec_b64 s[4:5], vcc
	s_xor_b64 s[36:37], exec, s[4:5]
	s_cbranch_execz .LBB0_1173
	v_readlane_b32 s4, v254, 7
	v_readlane_b32 s5, v254, 8
	s_waitcnt lgkmcnt(0)
	s_nop 3
	global_load_dword v2, v67, s[4:5] sc1
	s_waitcnt vmcnt(0)
	v_cmp_eq_u32_e32 vcc, v2, v3
	s_and_saveexec_b64 s[38:39], vcc
	s_cbranch_execz .LBB0_1172
	s_mov_b32 s3, 1
	s_mov_b64 s[42:43], 0
	s_branch .LBB0_1163

.LBB0_1417:
	s_or_b64 exec, exec, s[26:27]
	v_cvt_f32_u32_e32 v6, v4
	buffer_inv sc1
	s_waitcnt vmcnt(1)
	v_readfirstlane_b32 s3, v5
	v_sub_u32_e32 v5, 0, v4
	v_rcp_iflag_f32_e32 v6, v6
	v_add_u32_e32 v7, s3, v3
	v_mul_f32_e32 v6, 0x4f7ffffe, v6
	v_cvt_u32_f32_e32 v6, v6
	v_mul_lo_u32 v3, v5, v6
	v_mul_hi_u32 v3, v6, v3
	v_add_u32_e32 v3, v6, v3
	v_mul_hi_u32 v3, v7, v3
	v_mul_lo_u32 v5, v3, v4
	v_sub_u32_e32 v5, v7, v5
	v_add_u32_e32 v6, 1, v3
	v_cmp_ge_u32_e32 vcc, v5, v4
	s_nop 1
	v_cndmask_b32_e32 v3, v3, v6, vcc
	v_sub_u32_e32 v6, v5, v4
	v_cndmask_b32_e32 v5, v5, v6, vcc
	v_add_u32_e32 v6, 1, v3
	v_cmp_ge_u32_e32 vcc, v5, v4
	v_add_u32_e32 v5, 1, v7
	s_nop 0
	v_cndmask_b32_e32 v3, v3, v6, vcc
	v_mul_lo_u32 v6, v4, v3
	v_add_u32_e32 v4, v6, v4
	v_cmp_ne_u32_e32 vcc, v5, v4
	s_and_saveexec_b64 s[4:5], vcc
	s_xor_b64 s[36:37], exec, s[4:5]
	s_cbranch_execz .LBB0_1431
	v_readlane_b32 s4, v254, 7
	v_readlane_b32 s5, v254, 8
	s_waitcnt lgkmcnt(0)
	s_nop 3
	global_load_dword v2, v67, s[4:5] sc1
	s_waitcnt vmcnt(0)
	v_cmp_eq_u32_e32 vcc, v2, v3
	s_and_saveexec_b64 s[40:41], vcc
	s_cbranch_execz .LBB0_1430
	s_mov_b32 s3, 1
	s_mov_b64 s[42:43], 0
	s_branch .LBB0_1421

.LBB0_1430:
	s_or_b64 exec, exec, s[40:41]
	s_waitcnt vmcnt(0)
	s_waitcnt vmcnt(0)
